# differential attention: the 7 loop-invariant Q fragments kept in unused VGPRs instead of a per-wave LDS image re-read every tile (7 fewer ds_read_b128 per wave per tile); QK^T back to one-slice-ahead
# speedup vs baseline: 1.0074x; 1.0074x over previous
.LBB0_554:
	s_or_b64 exec, exec, s[4:5]
	s_ashr_i32 s95, s94, 31
	s_add_u32 s4, s2, s16
	s_addc_u32 s3, s3, 0
	v_mov_b32_e32 v38, v165
	s_add_u32 s2, s4, 0x2800
	s_addc_u32 s33, s3, 0
	v_readfirstlane_b32 s5, v38
	s_ashr_i32 s79, s5, 6
	v_bfe_u32 v0, v38, 5, 1
	v_and_b32_e32 v175, 31, v38
	s_lshl_b32 s92, s79, 5
	v_lshlrev_b32_e32 v32, 2, v0
	s_add_i32 s82, s92, s78
	v_sub_u32_e32 v1, v175, v32
	v_lshlrev_b32_e32 v176, 4, v0
	s_lshl_b32 s76, s79, 3
	v_bfe_u32 v0, v38, 4, 2
	v_writelane_b32 v255, s16, 17
	v_add_u32_e32 v179, s82, v1
	v_or_b32_e32 v1, s76, v0
	v_and_b32_e32 v2, 15, v38
	s_lshl_b32 s5, s79, 12
	v_and_b32_e32 v39, 63, v38
	v_bitop3_b32 v3, v0, v38, 15 bitop3:0x78
	v_mul_lo_u32 v1, v1, s84
	v_bitop3_b32 v0, v0, v2, 4 bitop3:0x36
	s_add_i32 s93, s5, s77
	s_mul_i32 s5, s79, 0x1c00
	v_readlane_b32 s7, v255, 51
	s_waitcnt vmcnt(16)
	v_lshlrev_b32_e32 v40, 4, v39
	v_lshl_or_b32 v0, v0, 4, v1
	s_lshl_b32 s83, s79, 11
	v_readlane_b32 s6, v255, 53
	s_add_i32 s5, s7, s5
	v_lshl_or_b32 v160, v3, 4, v1
	v_add_u32_e32 v170, 0x1a000, v0
	s_add_i32 s83, s83, s6
	v_add_u32_e32 v180, s5, v40
	s_waitcnt vmcnt(16) lgkmcnt(0)
	v_mov_b64_e32 v[218:219], v[128:129]
	v_mov_b64_e32 v[220:221], v[130:131]
	v_mov_b64_e32 v[222:223], v[132:133]
	v_mov_b64_e32 v[224:225], v[134:135]
	v_mov_b64_e32 v[230:231], v[136:137]
	v_mov_b64_e32 v[232:233], v[138:139]
	v_mov_b64_e32 v[234:235], v[140:141]
	v_mov_b64_e32 v[236:237], v[142:143]
	v_mov_b64_e32 v[238:239], v[144:145]
	v_mov_b64_e32 v[240:241], v[146:147]
	v_mov_b64_e32 v[242:243], v[148:149]
	v_mov_b64_e32 v[244:245], v[150:151]
	v_mov_b64_e32 v[246:247], v[152:153]
	v_mov_b64_e32 v[248:249], v[154:155]
	s_add_u32 s4, s4, 0x1a2800
	s_addc_u32 s5, s3, 0
	v_lshl_add_u64 v[0:1], s[4:5], 0, v[160:161]
	s_add_i32 s84, s83, 0x4000
	s_mov_b32 s3, m0
	s_mov_b32 m0, s84
	s_nop 0
	global_load_lds_dwordx4 v[0:1], off
	s_mov_b32 m0, s3
	v_mov_b32_e32 v171, v161
	v_lshl_add_u64 v[0:1], s[4:5], 0, v[170:171]
	s_add_i32 s85, s83, 0x4400
	s_mov_b32 s3, m0
	s_mov_b32 m0, s85
	s_nop 0
	global_load_lds_dwordx4 v[0:1], off
	s_mov_b32 m0, s3
	s_waitcnt lgkmcnt(0)
	s_barrier
	v_lshlrev_b32_e32 v0, 4, v38
	s_movk_i32 s3, 0x70
	v_lshlrev_b32_e32 v33, 8, v175
	v_and_b32_e32 v1, 0x70, v0
	v_bitop3_b32 v34, v176, v0, s3 bitop3:0x78
	s_movk_i32 s3, 0x60
	v_add_u32_e32 v2, s6, v33
	v_bitop3_b32 v35, v176, v1, 32 bitop3:0x36
	v_bitop3_b32 v36, v176, v1, 64 bitop3:0x36
	v_bitop3_b32 v37, v176, v1, s3 bitop3:0x36
	v_add_u32_e32 v181, v34, v2
	v_add_u32_e32 v182, v35, v2
	v_add_u32_e32 v183, v36, v2
	v_add_u32_e32 v184, v37, v2
	ds_read_b128 v[0:3], v181 offset:0
	ds_read_b128 v[4:7], v181 offset:0x2000
	ds_read_b128 v[42:45], v182 offset:0
	ds_read_b128 v[46:49], v182 offset:0x2000
	s_waitcnt lgkmcnt(2)
	s_nop 0
	v_mfma_f32_32x32x16_bf16 v[16:31], v[0:3], v[218:221], 0
	v_mfma_f32_32x32x16_bf16 v[0:15], v[4:7], v[218:221], 0
	ds_read_b128 v[54:57], v183 offset:0
	ds_read_b128 v[58:61], v183 offset:0x2000
	s_waitcnt lgkmcnt(2)
	v_mfma_f32_32x32x16_bf16 v[16:31], v[42:45], v[222:225], v[16:31]
	v_mfma_f32_32x32x16_bf16 v[0:15], v[46:49], v[222:225], v[0:15]
	ds_read_b128 v[42:45], v184 offset:0
	ds_read_b128 v[46:49], v184 offset:0x2000
	s_waitcnt lgkmcnt(2)
	v_mfma_f32_32x32x16_bf16 v[16:31], v[54:57], v[230:233], v[16:31]
	v_mfma_f32_32x32x16_bf16 v[0:15], v[58:61], v[230:233], v[0:15]
	ds_read_b128 v[54:57], v181 offset:0x80
	ds_read_b128 v[58:61], v181 offset:0x2080
	s_waitcnt lgkmcnt(2)
	v_mfma_f32_32x32x16_bf16 v[16:31], v[42:45], v[234:237], v[16:31]
	v_mfma_f32_32x32x16_bf16 v[0:15], v[46:49], v[234:237], v[0:15]
	ds_read_b128 v[42:45], v182 offset:0x80
	ds_read_b128 v[46:49], v182 offset:0x2080
	s_waitcnt lgkmcnt(2)
	v_mfma_f32_32x32x16_bf16 v[16:31], v[54:57], v[238:241], v[16:31]
	v_mfma_f32_32x32x16_bf16 v[0:15], v[58:61], v[238:241], v[0:15]
	ds_read_b128 v[54:57], v183 offset:0x80
	ds_read_b128 v[58:61], v183 offset:0x2080
	s_waitcnt lgkmcnt(2)
	v_mfma_f32_32x32x16_bf16 v[16:31], v[42:45], v[242:245], v[16:31]
	v_mfma_f32_32x32x16_bf16 v[0:15], v[46:49], v[242:245], v[0:15]
	ds_read_b128 v[42:45], v184 offset:0x80
	ds_read_b128 v[46:49], v184 offset:0x2080
	s_waitcnt lgkmcnt(2)
	v_mfma_f32_32x32x16_bf16 v[16:31], v[54:57], v[246:249], v[16:31]
	v_mfma_f32_32x32x16_bf16 v[0:15], v[58:61], v[246:249], v[0:15]
	s_waitcnt lgkmcnt(0)
	v_mfma_f32_32x32x16_bf16 v[16:31], v[42:45], v[166:169], v[16:31]
	v_mfma_f32_32x32x16_bf16 v[0:15], v[46:49], v[166:169], v[0:15]
	s_bitcmp0_b32 s100, 8
	s_cbranch_scc1 .Lstg_a9
	s_waitcnt vmcnt(0)
	s_waitcnt lgkmcnt(0)
	s_barrier
	s_sleep 5

.LBB0_557:
	ds_read_b64_tr_b16 v[144:145], v177 offset:0
	ds_read_b64_tr_b16 v[146:147], v177 offset:0x1000
	ds_read_b64_tr_b16 v[148:149], v177 offset:0x2000
	ds_read_b64_tr_b16 v[150:151], v177 offset:0x3000
	ds_read_b64_tr_b16 v[152:153], v177 offset:0x4000
	ds_read_b64_tr_b16 v[154:155], v177 offset:0x5000
	ds_read_b64_tr_b16 v[156:157], v177 offset:0x6000
	ds_read_b64_tr_b16 v[158:159], v177 offset:0x7000
	s_waitcnt lgkmcnt(6)
	s_nop 0
	v_mfma_f32_32x32x16_bf16 v[112:127], v[144:147], v[128:131], v[112:127]
	ds_read_b64_tr_b16 v[192:193], v177 offset:0x200
	ds_read_b64_tr_b16 v[194:195], v177 offset:0x1200
	s_waitcnt lgkmcnt(6)
	v_mfma_f32_32x32x16_bf16 v[112:127], v[148:151], v[132:135], v[112:127]
	ds_read_b64_tr_b16 v[196:197], v177 offset:0x2200
	ds_read_b64_tr_b16 v[198:199], v177 offset:0x3200
	s_waitcnt lgkmcnt(6)
	v_mfma_f32_32x32x16_bf16 v[112:127], v[152:155], v[136:139], v[112:127]
	ds_read_b64_tr_b16 v[200:201], v177 offset:0x4200
	ds_read_b64_tr_b16 v[202:203], v177 offset:0x5200
	s_waitcnt lgkmcnt(6)
	v_mfma_f32_32x32x16_bf16 v[112:127], v[156:159], v[140:143], v[112:127]
	ds_read_b64_tr_b16 v[204:205], v177 offset:0x6200
	ds_read_b64_tr_b16 v[206:207], v177 offset:0x7200
	s_waitcnt lgkmcnt(6)
	v_mfma_f32_32x32x16_bf16 v[80:95], v[192:195], v[128:131], v[80:95]
	ds_read_b64_tr_b16 v[144:145], v177 offset:0x400
	ds_read_b64_tr_b16 v[146:147], v177 offset:0x1400
	s_waitcnt lgkmcnt(6)
	v_mfma_f32_32x32x16_bf16 v[80:95], v[196:199], v[132:135], v[80:95]
	ds_read_b64_tr_b16 v[148:149], v177 offset:0x2400
	ds_read_b64_tr_b16 v[150:151], v177 offset:0x3400
	s_waitcnt lgkmcnt(6)
	v_mfma_f32_32x32x16_bf16 v[80:95], v[200:203], v[136:139], v[80:95]
	ds_read_b64_tr_b16 v[152:153], v177 offset:0x4400
	ds_read_b64_tr_b16 v[154:155], v177 offset:0x5400
	s_waitcnt lgkmcnt(6)
	v_mfma_f32_32x32x16_bf16 v[80:95], v[204:207], v[140:143], v[80:95]
	ds_read_b64_tr_b16 v[156:157], v177 offset:0x6400
	ds_read_b64_tr_b16 v[158:159], v177 offset:0x7400
	s_waitcnt lgkmcnt(6)
	v_mfma_f32_32x32x16_bf16 v[96:111], v[144:147], v[128:131], v[96:111]
	ds_read_b64_tr_b16 v[192:193], v177 offset:0x600
	ds_read_b64_tr_b16 v[194:195], v177 offset:0x1600
	s_waitcnt lgkmcnt(6)
	v_mfma_f32_32x32x16_bf16 v[96:111], v[148:151], v[132:135], v[96:111]
	ds_read_b64_tr_b16 v[196:197], v177 offset:0x2600
	ds_read_b64_tr_b16 v[198:199], v177 offset:0x3600
	s_waitcnt lgkmcnt(6)
	v_mfma_f32_32x32x16_bf16 v[96:111], v[152:155], v[136:139], v[96:111]
	ds_read_b64_tr_b16 v[200:201], v177 offset:0x4600
	ds_read_b64_tr_b16 v[202:203], v177 offset:0x5600
	s_waitcnt lgkmcnt(6)
	v_mfma_f32_32x32x16_bf16 v[96:111], v[156:159], v[140:143], v[96:111]
	ds_read_b64_tr_b16 v[204:205], v177 offset:0x6600
	ds_read_b64_tr_b16 v[206:207], v177 offset:0x7600
	s_waitcnt lgkmcnt(6)
	v_mfma_f32_32x32x16_bf16 v[64:79], v[192:195], v[128:131], v[64:79]
	ds_read_b64_tr_b16 v[144:145], v177 offset:0x800
	ds_read_b64_tr_b16 v[146:147], v177 offset:0x1800
	s_waitcnt lgkmcnt(6)
	v_mfma_f32_32x32x16_bf16 v[64:79], v[196:199], v[132:135], v[64:79]
	ds_read_b64_tr_b16 v[148:149], v177 offset:0x2800
	ds_read_b64_tr_b16 v[150:151], v177 offset:0x3800
	s_waitcnt lgkmcnt(6)
	v_mfma_f32_32x32x16_bf16 v[64:79], v[200:203], v[136:139], v[64:79]
	ds_read_b64_tr_b16 v[152:153], v177 offset:0x4800
	ds_read_b64_tr_b16 v[154:155], v177 offset:0x5800
	s_waitcnt lgkmcnt(6)
	v_mfma_f32_32x32x16_bf16 v[64:79], v[204:207], v[140:143], v[64:79]
	ds_read_b64_tr_b16 v[156:157], v177 offset:0x6800
	ds_read_b64_tr_b16 v[158:159], v177 offset:0x7800
	s_waitcnt lgkmcnt(6)
	v_mfma_f32_32x32x16_bf16 v[48:63], v[144:147], v[128:131], v[48:63]
	ds_read_b64_tr_b16 v[192:193], v177 offset:0xa00
	ds_read_b64_tr_b16 v[194:195], v177 offset:0x1a00
	s_waitcnt lgkmcnt(6)
	v_mfma_f32_32x32x16_bf16 v[48:63], v[148:151], v[132:135], v[48:63]
	ds_read_b64_tr_b16 v[196:197], v177 offset:0x2a00
	ds_read_b64_tr_b16 v[198:199], v177 offset:0x3a00
	s_waitcnt lgkmcnt(6)
	v_mfma_f32_32x32x16_bf16 v[48:63], v[152:155], v[136:139], v[48:63]
	ds_read_b64_tr_b16 v[200:201], v177 offset:0x4a00
	ds_read_b64_tr_b16 v[202:203], v177 offset:0x5a00
	s_waitcnt lgkmcnt(6)
	v_mfma_f32_32x32x16_bf16 v[48:63], v[156:159], v[140:143], v[48:63]
	ds_read_b64_tr_b16 v[204:205], v177 offset:0x6a00
	ds_read_b64_tr_b16 v[206:207], v177 offset:0x7a00
	s_waitcnt lgkmcnt(6)
	v_mfma_f32_32x32x16_bf16 v[32:47], v[192:195], v[128:131], v[32:47]
	ds_read_b64_tr_b16 v[144:145], v177 offset:0xc00
	ds_read_b64_tr_b16 v[146:147], v177 offset:0x1c00
	s_waitcnt lgkmcnt(6)
	v_mfma_f32_32x32x16_bf16 v[32:47], v[196:199], v[132:135], v[32:47]
	ds_read_b64_tr_b16 v[148:149], v177 offset:0x2c00
	ds_read_b64_tr_b16 v[150:151], v177 offset:0x3c00
	s_waitcnt lgkmcnt(6)
	v_mfma_f32_32x32x16_bf16 v[32:47], v[200:203], v[136:139], v[32:47]
	ds_read_b64_tr_b16 v[152:153], v177 offset:0x4c00
	ds_read_b64_tr_b16 v[154:155], v177 offset:0x5c00
	s_waitcnt lgkmcnt(6)
	v_mfma_f32_32x32x16_bf16 v[32:47], v[204:207], v[140:143], v[32:47]
	ds_read_b64_tr_b16 v[156:157], v177 offset:0x6c00
	ds_read_b64_tr_b16 v[158:159], v177 offset:0x7c00
	s_waitcnt lgkmcnt(6)
	v_mfma_f32_32x32x16_bf16 v[16:31], v[144:147], v[128:131], v[16:31]
	ds_read_b64_tr_b16 v[192:193], v177 offset:0xe00
	ds_read_b64_tr_b16 v[194:195], v177 offset:0x1e00
	s_waitcnt lgkmcnt(6)
	v_mfma_f32_32x32x16_bf16 v[16:31], v[148:151], v[132:135], v[16:31]
	ds_read_b64_tr_b16 v[196:197], v177 offset:0x2e00
	ds_read_b64_tr_b16 v[198:199], v177 offset:0x3e00
	s_waitcnt lgkmcnt(6)
	v_mfma_f32_32x32x16_bf16 v[16:31], v[152:155], v[136:139], v[16:31]
	ds_read_b64_tr_b16 v[200:201], v177 offset:0x4e00
	ds_read_b64_tr_b16 v[202:203], v177 offset:0x5e00
	s_waitcnt lgkmcnt(6)
	v_mfma_f32_32x32x16_bf16 v[16:31], v[156:159], v[140:143], v[16:31]
	ds_read_b64_tr_b16 v[204:205], v177 offset:0x6e00
	ds_read_b64_tr_b16 v[206:207], v177 offset:0x7e00
	s_waitcnt lgkmcnt(6)
	v_mfma_f32_32x32x16_bf16 v[0:15], v[192:195], v[128:131], v[0:15]
	s_waitcnt lgkmcnt(4)
	v_mfma_f32_32x32x16_bf16 v[0:15], v[196:199], v[132:135], v[0:15]
	s_waitcnt lgkmcnt(2)
	v_mfma_f32_32x32x16_bf16 v[0:15], v[200:203], v[136:139], v[0:15]
	s_waitcnt lgkmcnt(0)
	v_mfma_f32_32x32x16_bf16 v[0:15], v[204:207], v[140:143], v[0:15]
	ds_read_b128 v[128:131], v188 offset:0
	ds_read_b128 v[132:135], v188 offset:0x2000
	ds_read_b128 v[192:195], v187 offset:0
	ds_read_b128 v[196:199], v187 offset:0x2000
	s_waitcnt lgkmcnt(2)
	s_nop 0
	v_mfma_f32_32x32x16_bf16 v[144:159], v[128:131], v[218:221], 0
	v_mfma_f32_32x32x16_bf16 v[128:143], v[132:135], v[218:221], 0
	ds_read_b128 v[204:207], v186 offset:0
	ds_read_b128 v[208:211], v186 offset:0x2000
	s_waitcnt lgkmcnt(2)
	v_mfma_f32_32x32x16_bf16 v[144:159], v[192:195], v[222:225], v[144:159]
	v_mfma_f32_32x32x16_bf16 v[128:143], v[196:199], v[222:225], v[128:143]
	ds_read_b128 v[192:195], v185 offset:0
	ds_read_b128 v[196:199], v185 offset:0x2000
	s_waitcnt lgkmcnt(2)
	v_mfma_f32_32x32x16_bf16 v[144:159], v[204:207], v[230:233], v[144:159]
	v_mfma_f32_32x32x16_bf16 v[128:143], v[208:211], v[230:233], v[128:143]
	ds_read_b128 v[204:207], v188 offset:0x80
	ds_read_b128 v[208:211], v188 offset:0x2080
	s_waitcnt lgkmcnt(2)
	v_mfma_f32_32x32x16_bf16 v[144:159], v[192:195], v[234:237], v[144:159]
	v_mfma_f32_32x32x16_bf16 v[128:143], v[196:199], v[234:237], v[128:143]
	ds_read_b128 v[192:195], v187 offset:0x80
	ds_read_b128 v[196:199], v187 offset:0x2080
	s_waitcnt lgkmcnt(2)
	v_mfma_f32_32x32x16_bf16 v[144:159], v[204:207], v[238:241], v[144:159]
	v_mfma_f32_32x32x16_bf16 v[128:143], v[208:211], v[238:241], v[128:143]
	ds_read_b128 v[204:207], v186 offset:0x80
	ds_read_b128 v[208:211], v186 offset:0x2080
	s_waitcnt lgkmcnt(2)
	v_mfma_f32_32x32x16_bf16 v[144:159], v[192:195], v[242:245], v[144:159]
	v_mfma_f32_32x32x16_bf16 v[128:143], v[196:199], v[242:245], v[128:143]
	ds_read_b128 v[192:195], v185 offset:0x80
	ds_read_b128 v[196:199], v185 offset:0x2080
	s_waitcnt lgkmcnt(2)
	v_mfma_f32_32x32x16_bf16 v[144:159], v[204:207], v[246:249], v[144:159]
	v_mfma_f32_32x32x16_bf16 v[128:143], v[208:211], v[246:249], v[128:143]
	s_waitcnt lgkmcnt(0)
	v_mfma_f32_32x32x16_bf16 v[144:159], v[192:195], v[166:169], v[144:159]
	v_mfma_f32_32x32x16_bf16 v[128:143], v[196:199], v[166:169], v[128:143]
	s_bitcmp0_b32 s100, 8
	s_cbranch_scc1 .Lstg_a10
	s_waitcnt vmcnt(0)
	s_waitcnt lgkmcnt(0)
	s_barrier
	s_sleep 5

.LBB0_565:
	ds_read_b64_tr_b16 v[144:145], v177 offset:0x8000
	ds_read_b64_tr_b16 v[146:147], v177 offset:0x9000
	ds_read_b64_tr_b16 v[148:149], v177 offset:0xa000
	ds_read_b64_tr_b16 v[150:151], v177 offset:0xb000
	ds_read_b64_tr_b16 v[152:153], v177 offset:0xc000
	ds_read_b64_tr_b16 v[154:155], v177 offset:0xd000
	ds_read_b64_tr_b16 v[156:157], v177 offset:0xe000
	ds_read_b64_tr_b16 v[158:159], v177 offset:0xf000
	s_waitcnt lgkmcnt(6)
	s_nop 0
	v_mfma_f32_32x32x16_bf16 v[112:127], v[144:147], v[128:131], v[112:127]
	ds_read_b64_tr_b16 v[194:195], v177 offset:0x8200
	ds_read_b64_tr_b16 v[196:197], v177 offset:0x9200
	s_waitcnt lgkmcnt(6)
	v_mfma_f32_32x32x16_bf16 v[112:127], v[148:151], v[132:135], v[112:127]
	ds_read_b64_tr_b16 v[198:199], v177 offset:0xa200
	ds_read_b64_tr_b16 v[200:201], v177 offset:0xb200
	s_waitcnt lgkmcnt(6)
	v_mfma_f32_32x32x16_bf16 v[112:127], v[152:155], v[136:139], v[112:127]
	ds_read_b64_tr_b16 v[202:203], v177 offset:0xc200
	ds_read_b64_tr_b16 v[204:205], v177 offset:0xd200
	s_waitcnt lgkmcnt(6)
	v_mfma_f32_32x32x16_bf16 v[112:127], v[156:159], v[140:143], v[112:127]
	ds_read_b64_tr_b16 v[206:207], v177 offset:0xe200
	ds_read_b64_tr_b16 v[208:209], v177 offset:0xf200
	s_waitcnt lgkmcnt(6)
	v_mfma_f32_32x32x16_bf16 v[80:95], v[194:197], v[128:131], v[80:95]
	ds_read_b64_tr_b16 v[144:145], v177 offset:0x8400
	ds_read_b64_tr_b16 v[146:147], v177 offset:0x9400
	s_waitcnt lgkmcnt(6)
	v_mfma_f32_32x32x16_bf16 v[80:95], v[198:201], v[132:135], v[80:95]
	ds_read_b64_tr_b16 v[148:149], v177 offset:0xa400
	ds_read_b64_tr_b16 v[150:151], v177 offset:0xb400
	s_waitcnt lgkmcnt(6)
	v_mfma_f32_32x32x16_bf16 v[80:95], v[202:205], v[136:139], v[80:95]
	ds_read_b64_tr_b16 v[152:153], v177 offset:0xc400
	ds_read_b64_tr_b16 v[154:155], v177 offset:0xd400
	s_waitcnt lgkmcnt(6)
	v_mfma_f32_32x32x16_bf16 v[80:95], v[206:209], v[140:143], v[80:95]
	ds_read_b64_tr_b16 v[156:157], v177 offset:0xe400
	ds_read_b64_tr_b16 v[158:159], v177 offset:0xf400
	s_waitcnt lgkmcnt(6)
	v_mfma_f32_32x32x16_bf16 v[96:111], v[144:147], v[128:131], v[96:111]
	ds_read_b64_tr_b16 v[194:195], v177 offset:0x8600
	ds_read_b64_tr_b16 v[196:197], v177 offset:0x9600
	s_waitcnt lgkmcnt(6)
	v_mfma_f32_32x32x16_bf16 v[96:111], v[148:151], v[132:135], v[96:111]
	ds_read_b64_tr_b16 v[198:199], v177 offset:0xa600
	ds_read_b64_tr_b16 v[200:201], v177 offset:0xb600
	s_waitcnt lgkmcnt(6)
	v_mfma_f32_32x32x16_bf16 v[96:111], v[152:155], v[136:139], v[96:111]
	ds_read_b64_tr_b16 v[202:203], v177 offset:0xc600
	ds_read_b64_tr_b16 v[204:205], v177 offset:0xd600
	s_waitcnt lgkmcnt(6)
	v_mfma_f32_32x32x16_bf16 v[96:111], v[156:159], v[140:143], v[96:111]
	ds_read_b64_tr_b16 v[206:207], v177 offset:0xe600
	ds_read_b64_tr_b16 v[208:209], v177 offset:0xf600
	s_waitcnt lgkmcnt(6)
	v_mfma_f32_32x32x16_bf16 v[64:79], v[194:197], v[128:131], v[64:79]
	ds_read_b64_tr_b16 v[144:145], v177 offset:0x8800
	ds_read_b64_tr_b16 v[146:147], v177 offset:0x9800
	s_waitcnt lgkmcnt(6)
	v_mfma_f32_32x32x16_bf16 v[64:79], v[198:201], v[132:135], v[64:79]
	ds_read_b64_tr_b16 v[148:149], v177 offset:0xa800
	ds_read_b64_tr_b16 v[150:151], v177 offset:0xb800
	s_waitcnt lgkmcnt(6)
	v_mfma_f32_32x32x16_bf16 v[64:79], v[202:205], v[136:139], v[64:79]
	ds_read_b64_tr_b16 v[152:153], v177 offset:0xc800
	ds_read_b64_tr_b16 v[154:155], v177 offset:0xd800
	s_waitcnt lgkmcnt(6)
	v_mfma_f32_32x32x16_bf16 v[64:79], v[206:209], v[140:143], v[64:79]
	ds_read_b64_tr_b16 v[156:157], v177 offset:0xe800
	ds_read_b64_tr_b16 v[158:159], v177 offset:0xf800
	s_waitcnt lgkmcnt(6)
	v_mfma_f32_32x32x16_bf16 v[48:63], v[144:147], v[128:131], v[48:63]
	ds_read_b64_tr_b16 v[194:195], v177 offset:0x8a00
	ds_read_b64_tr_b16 v[196:197], v177 offset:0x9a00
	s_waitcnt lgkmcnt(6)
	v_mfma_f32_32x32x16_bf16 v[48:63], v[148:151], v[132:135], v[48:63]
	ds_read_b64_tr_b16 v[198:199], v177 offset:0xaa00
	ds_read_b64_tr_b16 v[200:201], v177 offset:0xba00
	s_waitcnt lgkmcnt(6)
	v_mfma_f32_32x32x16_bf16 v[48:63], v[152:155], v[136:139], v[48:63]
	ds_read_b64_tr_b16 v[202:203], v177 offset:0xca00
	ds_read_b64_tr_b16 v[204:205], v177 offset:0xda00
	s_waitcnt lgkmcnt(6)
	v_mfma_f32_32x32x16_bf16 v[48:63], v[156:159], v[140:143], v[48:63]
	ds_read_b64_tr_b16 v[206:207], v177 offset:0xea00
	ds_read_b64_tr_b16 v[208:209], v177 offset:0xfa00
	s_waitcnt lgkmcnt(6)
	v_mfma_f32_32x32x16_bf16 v[32:47], v[194:197], v[128:131], v[32:47]
	ds_read_b64_tr_b16 v[144:145], v177 offset:0x8c00
	ds_read_b64_tr_b16 v[146:147], v177 offset:0x9c00
	s_waitcnt lgkmcnt(6)
	v_mfma_f32_32x32x16_bf16 v[32:47], v[198:201], v[132:135], v[32:47]
	ds_read_b64_tr_b16 v[148:149], v177 offset:0xac00
	ds_read_b64_tr_b16 v[150:151], v177 offset:0xbc00
	s_waitcnt lgkmcnt(6)
	v_mfma_f32_32x32x16_bf16 v[32:47], v[202:205], v[136:139], v[32:47]
	ds_read_b64_tr_b16 v[152:153], v177 offset:0xcc00
	ds_read_b64_tr_b16 v[154:155], v177 offset:0xdc00
	s_waitcnt lgkmcnt(6)
	v_mfma_f32_32x32x16_bf16 v[32:47], v[206:209], v[140:143], v[32:47]
	ds_read_b64_tr_b16 v[156:157], v177 offset:0xec00
	ds_read_b64_tr_b16 v[158:159], v177 offset:0xfc00
	s_waitcnt lgkmcnt(6)
	v_mfma_f32_32x32x16_bf16 v[16:31], v[144:147], v[128:131], v[16:31]
	ds_read_b64_tr_b16 v[194:195], v177 offset:0x8e00
	ds_read_b64_tr_b16 v[196:197], v177 offset:0x9e00
	s_waitcnt lgkmcnt(6)
	v_mfma_f32_32x32x16_bf16 v[16:31], v[148:151], v[132:135], v[16:31]
	ds_read_b64_tr_b16 v[198:199], v177 offset:0xae00
	ds_read_b64_tr_b16 v[200:201], v177 offset:0xbe00
	s_waitcnt lgkmcnt(6)
	v_mfma_f32_32x32x16_bf16 v[16:31], v[152:155], v[136:139], v[16:31]
	ds_read_b64_tr_b16 v[202:203], v177 offset:0xce00
	ds_read_b64_tr_b16 v[204:205], v177 offset:0xde00
	s_waitcnt lgkmcnt(6)
	v_mfma_f32_32x32x16_bf16 v[16:31], v[156:159], v[140:143], v[16:31]
	ds_read_b64_tr_b16 v[206:207], v177 offset:0xee00
	ds_read_b64_tr_b16 v[208:209], v177 offset:0xfe00
	s_waitcnt lgkmcnt(6)
	v_mfma_f32_32x32x16_bf16 v[0:15], v[194:197], v[128:131], v[0:15]
	s_waitcnt lgkmcnt(4)
	v_mfma_f32_32x32x16_bf16 v[0:15], v[198:201], v[132:135], v[0:15]
	s_waitcnt lgkmcnt(2)
	v_mfma_f32_32x32x16_bf16 v[0:15], v[202:205], v[136:139], v[0:15]
	s_waitcnt lgkmcnt(0)
	v_mfma_f32_32x32x16_bf16 v[0:15], v[206:209], v[140:143], v[0:15]
	ds_read_b128 v[128:131], v181 offset:0
	ds_read_b128 v[132:135], v181 offset:0x2000
	ds_read_b128 v[194:197], v182 offset:0
	ds_read_b128 v[198:201], v182 offset:0x2000
	s_waitcnt lgkmcnt(2)
	s_nop 0
	v_mfma_f32_32x32x16_bf16 v[144:159], v[128:131], v[218:221], 0
	v_mfma_f32_32x32x16_bf16 v[128:143], v[132:135], v[218:221], 0
	ds_read_b128 v[206:209], v183 offset:0
	ds_read_b128 v[210:213], v183 offset:0x2000
	s_waitcnt lgkmcnt(2)
	v_mfma_f32_32x32x16_bf16 v[144:159], v[194:197], v[222:225], v[144:159]
	v_mfma_f32_32x32x16_bf16 v[128:143], v[198:201], v[222:225], v[128:143]
	ds_read_b128 v[194:197], v184 offset:0
	ds_read_b128 v[198:201], v184 offset:0x2000
	s_waitcnt lgkmcnt(2)
	v_mfma_f32_32x32x16_bf16 v[144:159], v[206:209], v[230:233], v[144:159]
	v_mfma_f32_32x32x16_bf16 v[128:143], v[210:213], v[230:233], v[128:143]
	ds_read_b128 v[206:209], v181 offset:0x80
	ds_read_b128 v[210:213], v181 offset:0x2080
	s_waitcnt lgkmcnt(2)
	v_mfma_f32_32x32x16_bf16 v[144:159], v[194:197], v[234:237], v[144:159]
	v_mfma_f32_32x32x16_bf16 v[128:143], v[198:201], v[234:237], v[128:143]
	ds_read_b128 v[194:197], v182 offset:0x80
	ds_read_b128 v[198:201], v182 offset:0x2080
	s_waitcnt lgkmcnt(2)
	v_mfma_f32_32x32x16_bf16 v[144:159], v[206:209], v[238:241], v[144:159]
	v_mfma_f32_32x32x16_bf16 v[128:143], v[210:213], v[238:241], v[128:143]
	ds_read_b128 v[206:209], v183 offset:0x80
	ds_read_b128 v[210:213], v183 offset:0x2080
	s_waitcnt lgkmcnt(2)
	v_mfma_f32_32x32x16_bf16 v[144:159], v[194:197], v[242:245], v[144:159]
	v_mfma_f32_32x32x16_bf16 v[128:143], v[198:201], v[242:245], v[128:143]
	ds_read_b128 v[194:197], v184 offset:0x80
	ds_read_b128 v[198:201], v184 offset:0x2080
	s_waitcnt lgkmcnt(2)
	v_mfma_f32_32x32x16_bf16 v[144:159], v[206:209], v[246:249], v[144:159]
	v_mfma_f32_32x32x16_bf16 v[128:143], v[210:213], v[246:249], v[128:143]
	s_waitcnt lgkmcnt(0)
	v_mfma_f32_32x32x16_bf16 v[144:159], v[194:197], v[166:169], v[144:159]
	v_mfma_f32_32x32x16_bf16 v[128:143], v[198:201], v[166:169], v[128:143]
	s_bitcmp0_b32 s100, 8
	s_cbranch_scc1 .Lstg_a11
	s_waitcnt vmcnt(0)
	s_waitcnt lgkmcnt(0)
	s_barrier
	s_sleep 5

.LBB0_580:
	ds_read_b64_tr_b16 v[144:145], v177 offset:0
	ds_read_b64_tr_b16 v[146:147], v177 offset:0x1000
	ds_read_b64_tr_b16 v[148:149], v177 offset:0x2000
	ds_read_b64_tr_b16 v[150:151], v177 offset:0x3000
	ds_read_b64_tr_b16 v[152:153], v177 offset:0x4000
	ds_read_b64_tr_b16 v[154:155], v177 offset:0x5000
	ds_read_b64_tr_b16 v[156:157], v177 offset:0x6000
	ds_read_b64_tr_b16 v[158:159], v177 offset:0x7000
	s_waitcnt lgkmcnt(6)
	s_nop 0
	v_mfma_f32_32x32x16_bf16 v[112:127], v[144:147], v[128:131], v[112:127]
	ds_read_b64_tr_b16 v[192:193], v177 offset:0x200
	ds_read_b64_tr_b16 v[194:195], v177 offset:0x1200
	s_waitcnt lgkmcnt(6)
	v_mfma_f32_32x32x16_bf16 v[112:127], v[148:151], v[132:135], v[112:127]
	ds_read_b64_tr_b16 v[196:197], v177 offset:0x2200
	ds_read_b64_tr_b16 v[198:199], v177 offset:0x3200
	s_waitcnt lgkmcnt(6)
	v_mfma_f32_32x32x16_bf16 v[112:127], v[152:155], v[136:139], v[112:127]
	ds_read_b64_tr_b16 v[200:201], v177 offset:0x4200
	ds_read_b64_tr_b16 v[202:203], v177 offset:0x5200
	s_waitcnt lgkmcnt(6)
	v_mfma_f32_32x32x16_bf16 v[112:127], v[156:159], v[140:143], v[112:127]
	ds_read_b64_tr_b16 v[204:205], v177 offset:0x6200
	ds_read_b64_tr_b16 v[206:207], v177 offset:0x7200
	s_waitcnt lgkmcnt(6)
	v_mfma_f32_32x32x16_bf16 v[80:95], v[192:195], v[128:131], v[80:95]
	ds_read_b64_tr_b16 v[144:145], v177 offset:0x400
	ds_read_b64_tr_b16 v[146:147], v177 offset:0x1400
	s_waitcnt lgkmcnt(6)
	v_mfma_f32_32x32x16_bf16 v[80:95], v[196:199], v[132:135], v[80:95]
	ds_read_b64_tr_b16 v[148:149], v177 offset:0x2400
	ds_read_b64_tr_b16 v[150:151], v177 offset:0x3400
	s_waitcnt lgkmcnt(6)
	v_mfma_f32_32x32x16_bf16 v[80:95], v[200:203], v[136:139], v[80:95]
	ds_read_b64_tr_b16 v[152:153], v177 offset:0x4400
	ds_read_b64_tr_b16 v[154:155], v177 offset:0x5400
	s_waitcnt lgkmcnt(6)
	v_mfma_f32_32x32x16_bf16 v[80:95], v[204:207], v[140:143], v[80:95]
	ds_read_b64_tr_b16 v[156:157], v177 offset:0x6400
	ds_read_b64_tr_b16 v[158:159], v177 offset:0x7400
	s_waitcnt lgkmcnt(6)
	v_mfma_f32_32x32x16_bf16 v[96:111], v[144:147], v[128:131], v[96:111]
	ds_read_b64_tr_b16 v[192:193], v177 offset:0x600
	ds_read_b64_tr_b16 v[194:195], v177 offset:0x1600
	s_waitcnt lgkmcnt(6)
	v_mfma_f32_32x32x16_bf16 v[96:111], v[148:151], v[132:135], v[96:111]
	ds_read_b64_tr_b16 v[196:197], v177 offset:0x2600
	ds_read_b64_tr_b16 v[198:199], v177 offset:0x3600
	s_waitcnt lgkmcnt(6)
	v_mfma_f32_32x32x16_bf16 v[96:111], v[152:155], v[136:139], v[96:111]
	ds_read_b64_tr_b16 v[200:201], v177 offset:0x4600
	ds_read_b64_tr_b16 v[202:203], v177 offset:0x5600
	s_waitcnt lgkmcnt(6)
	v_mfma_f32_32x32x16_bf16 v[96:111], v[156:159], v[140:143], v[96:111]
	ds_read_b64_tr_b16 v[204:205], v177 offset:0x6600
	ds_read_b64_tr_b16 v[206:207], v177 offset:0x7600
	s_waitcnt lgkmcnt(6)
	v_mfma_f32_32x32x16_bf16 v[64:79], v[192:195], v[128:131], v[64:79]
	ds_read_b64_tr_b16 v[144:145], v177 offset:0x800
	ds_read_b64_tr_b16 v[146:147], v177 offset:0x1800
	s_waitcnt lgkmcnt(6)
	v_mfma_f32_32x32x16_bf16 v[64:79], v[196:199], v[132:135], v[64:79]
	ds_read_b64_tr_b16 v[148:149], v177 offset:0x2800
	ds_read_b64_tr_b16 v[150:151], v177 offset:0x3800
	s_waitcnt lgkmcnt(6)
	v_mfma_f32_32x32x16_bf16 v[64:79], v[200:203], v[136:139], v[64:79]
	ds_read_b64_tr_b16 v[152:153], v177 offset:0x4800
	ds_read_b64_tr_b16 v[154:155], v177 offset:0x5800
	s_waitcnt lgkmcnt(6)
	v_mfma_f32_32x32x16_bf16 v[64:79], v[204:207], v[140:143], v[64:79]
	ds_read_b64_tr_b16 v[156:157], v177 offset:0x6800
	ds_read_b64_tr_b16 v[158:159], v177 offset:0x7800
	s_waitcnt lgkmcnt(6)
	v_mfma_f32_32x32x16_bf16 v[48:63], v[144:147], v[128:131], v[48:63]
	ds_read_b64_tr_b16 v[192:193], v177 offset:0xa00
	ds_read_b64_tr_b16 v[194:195], v177 offset:0x1a00
	s_waitcnt lgkmcnt(6)
	v_mfma_f32_32x32x16_bf16 v[48:63], v[148:151], v[132:135], v[48:63]
	ds_read_b64_tr_b16 v[196:197], v177 offset:0x2a00
	ds_read_b64_tr_b16 v[198:199], v177 offset:0x3a00
	s_waitcnt lgkmcnt(6)
	v_mfma_f32_32x32x16_bf16 v[48:63], v[152:155], v[136:139], v[48:63]
	ds_read_b64_tr_b16 v[200:201], v177 offset:0x4a00
	ds_read_b64_tr_b16 v[202:203], v177 offset:0x5a00
	s_waitcnt lgkmcnt(6)
	v_mfma_f32_32x32x16_bf16 v[48:63], v[156:159], v[140:143], v[48:63]
	ds_read_b64_tr_b16 v[204:205], v177 offset:0x6a00
	ds_read_b64_tr_b16 v[206:207], v177 offset:0x7a00
	s_waitcnt lgkmcnt(6)
	v_mfma_f32_32x32x16_bf16 v[32:47], v[192:195], v[128:131], v[32:47]
	ds_read_b64_tr_b16 v[144:145], v177 offset:0xc00
	ds_read_b64_tr_b16 v[146:147], v177 offset:0x1c00
	s_waitcnt lgkmcnt(6)
	v_mfma_f32_32x32x16_bf16 v[32:47], v[196:199], v[132:135], v[32:47]
	ds_read_b64_tr_b16 v[148:149], v177 offset:0x2c00
	ds_read_b64_tr_b16 v[150:151], v177 offset:0x3c00
	s_waitcnt lgkmcnt(6)
	v_mfma_f32_32x32x16_bf16 v[32:47], v[200:203], v[136:139], v[32:47]
	ds_read_b64_tr_b16 v[152:153], v177 offset:0x4c00
	ds_read_b64_tr_b16 v[154:155], v177 offset:0x5c00
	s_waitcnt lgkmcnt(6)
	v_mfma_f32_32x32x16_bf16 v[32:47], v[204:207], v[140:143], v[32:47]
	ds_read_b64_tr_b16 v[156:157], v177 offset:0x6c00
	ds_read_b64_tr_b16 v[158:159], v177 offset:0x7c00
	s_waitcnt lgkmcnt(6)
	v_mfma_f32_32x32x16_bf16 v[16:31], v[144:147], v[128:131], v[16:31]
	ds_read_b64_tr_b16 v[192:193], v177 offset:0xe00
	ds_read_b64_tr_b16 v[194:195], v177 offset:0x1e00
	s_waitcnt lgkmcnt(6)
	v_mfma_f32_32x32x16_bf16 v[16:31], v[148:151], v[132:135], v[16:31]
	ds_read_b64_tr_b16 v[196:197], v177 offset:0x2e00
	ds_read_b64_tr_b16 v[198:199], v177 offset:0x3e00
	s_waitcnt lgkmcnt(6)
	v_mfma_f32_32x32x16_bf16 v[16:31], v[152:155], v[136:139], v[16:31]
	ds_read_b64_tr_b16 v[200:201], v177 offset:0x4e00
	ds_read_b64_tr_b16 v[202:203], v177 offset:0x5e00
	s_waitcnt lgkmcnt(6)
	v_mfma_f32_32x32x16_bf16 v[16:31], v[156:159], v[140:143], v[16:31]
	ds_read_b64_tr_b16 v[204:205], v177 offset:0x6e00
	ds_read_b64_tr_b16 v[206:207], v177 offset:0x7e00
	s_waitcnt lgkmcnt(6)
	v_mfma_f32_32x32x16_bf16 v[0:15], v[192:195], v[128:131], v[0:15]
	s_waitcnt lgkmcnt(4)
	v_mfma_f32_32x32x16_bf16 v[0:15], v[196:199], v[132:135], v[0:15]
	s_waitcnt lgkmcnt(2)
	v_mfma_f32_32x32x16_bf16 v[0:15], v[200:203], v[136:139], v[0:15]
	s_waitcnt lgkmcnt(0)
	v_mfma_f32_32x32x16_bf16 v[0:15], v[204:207], v[140:143], v[0:15]
	ds_read_b128 v[128:131], v188 offset:0
	ds_read_b128 v[132:135], v188 offset:0x2000
	ds_read_b128 v[192:195], v187 offset:0
	ds_read_b128 v[196:199], v187 offset:0x2000
	s_waitcnt lgkmcnt(2)
	s_nop 0
	v_mfma_f32_32x32x16_bf16 v[144:159], v[128:131], v[218:221], 0
	v_mfma_f32_32x32x16_bf16 v[128:143], v[132:135], v[218:221], 0
	ds_read_b128 v[204:207], v186 offset:0
	ds_read_b128 v[208:211], v186 offset:0x2000
	s_waitcnt lgkmcnt(2)
	v_mfma_f32_32x32x16_bf16 v[144:159], v[192:195], v[222:225], v[144:159]
	v_mfma_f32_32x32x16_bf16 v[128:143], v[196:199], v[222:225], v[128:143]
	ds_read_b128 v[192:195], v185 offset:0
	ds_read_b128 v[196:199], v185 offset:0x2000
	s_waitcnt lgkmcnt(2)
	v_mfma_f32_32x32x16_bf16 v[144:159], v[204:207], v[230:233], v[144:159]
	v_mfma_f32_32x32x16_bf16 v[128:143], v[208:211], v[230:233], v[128:143]
	ds_read_b128 v[204:207], v188 offset:0x80
	ds_read_b128 v[208:211], v188 offset:0x2080
	s_waitcnt lgkmcnt(2)
	v_mfma_f32_32x32x16_bf16 v[144:159], v[192:195], v[234:237], v[144:159]
	v_mfma_f32_32x32x16_bf16 v[128:143], v[196:199], v[234:237], v[128:143]
	ds_read_b128 v[192:195], v187 offset:0x80
	ds_read_b128 v[196:199], v187 offset:0x2080
	s_waitcnt lgkmcnt(2)
	v_mfma_f32_32x32x16_bf16 v[144:159], v[204:207], v[238:241], v[144:159]
	v_mfma_f32_32x32x16_bf16 v[128:143], v[208:211], v[238:241], v[128:143]
	ds_read_b128 v[204:207], v186 offset:0x80
	ds_read_b128 v[208:211], v186 offset:0x2080
	s_waitcnt lgkmcnt(2)
	v_mfma_f32_32x32x16_bf16 v[144:159], v[192:195], v[242:245], v[144:159]
	v_mfma_f32_32x32x16_bf16 v[128:143], v[196:199], v[242:245], v[128:143]
	ds_read_b128 v[180:183], v185 offset:0x80
	ds_read_b128 v[192:195], v185 offset:0x2080
	s_waitcnt lgkmcnt(2)
	v_mfma_f32_32x32x16_bf16 v[144:159], v[204:207], v[246:249], v[144:159]
	v_mfma_f32_32x32x16_bf16 v[128:143], v[208:211], v[246:249], v[128:143]
	s_waitcnt lgkmcnt(0)
	v_mfma_f32_32x32x16_bf16 v[144:159], v[180:183], v[166:169], v[144:159]
	v_mfma_f32_32x32x16_bf16 v[128:143], v[192:195], v[166:169], v[128:143]
	s_bitcmp0_b32 s100, 8
	s_cbranch_scc1 .Lstg_a12
	s_waitcnt vmcnt(0)
	s_waitcnt lgkmcnt(0)
	s_barrier
	s_sleep 5

.LBB0_586:
	s_or_b64 exec, exec, s[4:5]
	v_mov_b32_e32 v38, v165
	v_readlane_b32 s5, v255, 51
	v_readfirstlane_b32 s2, v38
	s_ashr_i32 s79, s2, 6
	v_bfe_u32 v0, v38, 5, 1
	v_and_b32_e32 v176, 31, v38
	s_lshl_b32 s92, s79, 5
	v_lshlrev_b32_e32 v32, 2, v0
	s_add_i32 s74, s92, s74
	v_sub_u32_e32 v1, v176, v32
	v_lshlrev_b32_e32 v175, 4, v0
	s_lshl_b32 s2, s79, 3
	v_bfe_u32 v0, v38, 4, 2
	v_add_u32_e32 v179, s74, v1
	v_or_b32_e32 v1, s2, v0
	v_and_b32_e32 v2, 15, v38
	v_and_b32_e32 v39, 63, v38
	v_bitop3_b32 v3, v0, v38, 15 bitop3:0x78
	v_mul_lo_u32 v1, v1, s14
	v_bitop3_b32 v0, v0, v2, 4 bitop3:0x36
	s_mul_i32 s4, s79, 0x1c00
	s_waitcnt vmcnt(16)
	v_lshlrev_b32_e32 v40, 4, v39
	v_lshl_or_b32 v0, v0, 4, v1
	s_lshl_b32 s78, s79, 11
	v_readlane_b32 s7, v255, 53
	s_lshl_b32 s3, s79, 12
	s_add_i32 s4, s5, s4
	v_lshl_or_b32 v160, v3, 4, v1
	v_add_u32_e32 v170, 0x1a000, v0
	s_add_i32 s78, s78, s7
	s_add_i32 s3, s3, s33
	v_add_u32_e32 v180, s4, v40
	s_waitcnt vmcnt(16) lgkmcnt(0)
	v_mov_b64_e32 v[218:219], v[128:129]
	v_mov_b64_e32 v[220:221], v[130:131]
	v_mov_b64_e32 v[222:223], v[132:133]
	v_mov_b64_e32 v[224:225], v[134:135]
	v_mov_b64_e32 v[230:231], v[136:137]
	v_mov_b64_e32 v[232:233], v[138:139]
	v_mov_b64_e32 v[234:235], v[140:141]
	v_mov_b64_e32 v[236:237], v[142:143]
	v_mov_b64_e32 v[238:239], v[144:145]
	v_mov_b64_e32 v[240:241], v[146:147]
	v_mov_b64_e32 v[242:243], v[148:149]
	v_mov_b64_e32 v[244:245], v[150:151]
	v_mov_b64_e32 v[246:247], v[152:153]
	v_mov_b64_e32 v[248:249], v[154:155]
	s_add_u32 s4, s66, 0x1a2900
	s_addc_u32 s5, s67, 0
	v_lshl_add_u64 v[0:1], s[4:5], 0, v[160:161]
	s_add_i32 s82, s78, 0x4000
	s_mov_b32 s6, m0
	s_mov_b32 m0, s82
	s_nop 0
	global_load_lds_dwordx4 v[0:1], off
	s_mov_b32 m0, s6
	v_mov_b32_e32 v171, v161
	v_lshl_add_u64 v[0:1], s[4:5], 0, v[170:171]
	s_add_i32 s84, s78, 0x4400
	s_mov_b32 s4, m0
	s_mov_b32 m0, s84
	s_nop 0
	global_load_lds_dwordx4 v[0:1], off
	s_mov_b32 m0, s4
	s_waitcnt lgkmcnt(0)
	s_barrier
	v_lshlrev_b32_e32 v0, 4, v38
	s_movk_i32 s4, 0x70
	v_lshlrev_b32_e32 v33, 8, v176
	v_and_b32_e32 v1, 0x70, v0
	v_bitop3_b32 v34, v175, v0, s4 bitop3:0x78
	s_movk_i32 s4, 0x60
	v_add_u32_e32 v2, s7, v33
	v_bitop3_b32 v35, v175, v1, 32 bitop3:0x36
	v_bitop3_b32 v36, v175, v1, 64 bitop3:0x36
	v_bitop3_b32 v37, v175, v1, s4 bitop3:0x36
	v_add_u32_e32 v181, v34, v2
	v_add_u32_e32 v182, v35, v2
	v_add_u32_e32 v183, v36, v2
	v_add_u32_e32 v184, v37, v2
	ds_read_b128 v[0:3], v181 offset:0
	ds_read_b128 v[4:7], v181 offset:0x2000
	ds_read_b128 v[42:45], v182 offset:0
	ds_read_b128 v[46:49], v182 offset:0x2000
	s_waitcnt lgkmcnt(2)
	s_nop 0
	v_mfma_f32_32x32x16_bf16 v[16:31], v[0:3], v[218:221], 0
	v_mfma_f32_32x32x16_bf16 v[0:15], v[4:7], v[218:221], 0
	ds_read_b128 v[54:57], v183 offset:0
	ds_read_b128 v[58:61], v183 offset:0x2000
	s_waitcnt lgkmcnt(2)
	v_mfma_f32_32x32x16_bf16 v[16:31], v[42:45], v[222:225], v[16:31]
	v_mfma_f32_32x32x16_bf16 v[0:15], v[46:49], v[222:225], v[0:15]
	ds_read_b128 v[42:45], v184 offset:0
	ds_read_b128 v[46:49], v184 offset:0x2000
	s_waitcnt lgkmcnt(2)
	v_mfma_f32_32x32x16_bf16 v[16:31], v[54:57], v[230:233], v[16:31]
	v_mfma_f32_32x32x16_bf16 v[0:15], v[58:61], v[230:233], v[0:15]
	ds_read_b128 v[54:57], v181 offset:0x80
	ds_read_b128 v[58:61], v181 offset:0x2080
	s_waitcnt lgkmcnt(2)
	v_mfma_f32_32x32x16_bf16 v[16:31], v[42:45], v[234:237], v[16:31]
	v_mfma_f32_32x32x16_bf16 v[0:15], v[46:49], v[234:237], v[0:15]
	ds_read_b128 v[42:45], v182 offset:0x80
	ds_read_b128 v[46:49], v182 offset:0x2080
	s_waitcnt lgkmcnt(2)
	v_mfma_f32_32x32x16_bf16 v[16:31], v[54:57], v[238:241], v[16:31]
	v_mfma_f32_32x32x16_bf16 v[0:15], v[58:61], v[238:241], v[0:15]
	ds_read_b128 v[54:57], v183 offset:0x80
	ds_read_b128 v[58:61], v183 offset:0x2080
	s_waitcnt lgkmcnt(2)
	v_mfma_f32_32x32x16_bf16 v[16:31], v[42:45], v[242:245], v[16:31]
	v_mfma_f32_32x32x16_bf16 v[0:15], v[46:49], v[242:245], v[0:15]
	ds_read_b128 v[42:45], v184 offset:0x80
	ds_read_b128 v[46:49], v184 offset:0x2080
	s_waitcnt lgkmcnt(2)
	v_mfma_f32_32x32x16_bf16 v[16:31], v[54:57], v[246:249], v[16:31]
	v_mfma_f32_32x32x16_bf16 v[0:15], v[58:61], v[246:249], v[0:15]
	s_waitcnt lgkmcnt(0)
	v_mfma_f32_32x32x16_bf16 v[16:31], v[42:45], v[166:169], v[16:31]
	v_mfma_f32_32x32x16_bf16 v[0:15], v[46:49], v[166:169], v[0:15]
	s_bitcmp0_b32 s100, 8
	s_cbranch_scc1 .Lstg_a17
	s_waitcnt vmcnt(0)
	s_waitcnt lgkmcnt(0)
	s_barrier
	s_sleep 5

.LBB0_589:
	ds_read_b64_tr_b16 v[144:145], v177 offset:0
	ds_read_b64_tr_b16 v[146:147], v177 offset:0x1000
	ds_read_b64_tr_b16 v[148:149], v177 offset:0x2000
	ds_read_b64_tr_b16 v[150:151], v177 offset:0x3000
	ds_read_b64_tr_b16 v[152:153], v177 offset:0x4000
	ds_read_b64_tr_b16 v[154:155], v177 offset:0x5000
	ds_read_b64_tr_b16 v[156:157], v177 offset:0x6000
	ds_read_b64_tr_b16 v[158:159], v177 offset:0x7000
	s_waitcnt lgkmcnt(6)
	s_nop 0
	v_mfma_f32_32x32x16_bf16 v[112:127], v[144:147], v[128:131], v[112:127]
	ds_read_b64_tr_b16 v[192:193], v177 offset:0x200
	ds_read_b64_tr_b16 v[194:195], v177 offset:0x1200
	s_waitcnt lgkmcnt(6)
	v_mfma_f32_32x32x16_bf16 v[112:127], v[148:151], v[132:135], v[112:127]
	ds_read_b64_tr_b16 v[196:197], v177 offset:0x2200
	ds_read_b64_tr_b16 v[198:199], v177 offset:0x3200
	s_waitcnt lgkmcnt(6)
	v_mfma_f32_32x32x16_bf16 v[112:127], v[152:155], v[136:139], v[112:127]
	ds_read_b64_tr_b16 v[200:201], v177 offset:0x4200
	ds_read_b64_tr_b16 v[202:203], v177 offset:0x5200
	s_waitcnt lgkmcnt(6)
	v_mfma_f32_32x32x16_bf16 v[112:127], v[156:159], v[140:143], v[112:127]
	ds_read_b64_tr_b16 v[204:205], v177 offset:0x6200
	ds_read_b64_tr_b16 v[206:207], v177 offset:0x7200
	s_waitcnt lgkmcnt(6)
	v_mfma_f32_32x32x16_bf16 v[96:111], v[192:195], v[128:131], v[96:111]
	ds_read_b64_tr_b16 v[144:145], v177 offset:0x400
	ds_read_b64_tr_b16 v[146:147], v177 offset:0x1400
	s_waitcnt lgkmcnt(6)
	v_mfma_f32_32x32x16_bf16 v[96:111], v[196:199], v[132:135], v[96:111]
	ds_read_b64_tr_b16 v[148:149], v177 offset:0x2400
	ds_read_b64_tr_b16 v[150:151], v177 offset:0x3400
	s_waitcnt lgkmcnt(6)
	v_mfma_f32_32x32x16_bf16 v[96:111], v[200:203], v[136:139], v[96:111]
	ds_read_b64_tr_b16 v[152:153], v177 offset:0x4400
	ds_read_b64_tr_b16 v[154:155], v177 offset:0x5400
	s_waitcnt lgkmcnt(6)
	v_mfma_f32_32x32x16_bf16 v[96:111], v[204:207], v[140:143], v[96:111]
	ds_read_b64_tr_b16 v[156:157], v177 offset:0x6400
	ds_read_b64_tr_b16 v[158:159], v177 offset:0x7400
	s_waitcnt lgkmcnt(6)
	v_mfma_f32_32x32x16_bf16 v[80:95], v[144:147], v[128:131], v[80:95]
	ds_read_b64_tr_b16 v[192:193], v177 offset:0x600
	ds_read_b64_tr_b16 v[194:195], v177 offset:0x1600
	s_waitcnt lgkmcnt(6)
	v_mfma_f32_32x32x16_bf16 v[80:95], v[148:151], v[132:135], v[80:95]
	ds_read_b64_tr_b16 v[196:197], v177 offset:0x2600
	ds_read_b64_tr_b16 v[198:199], v177 offset:0x3600
	s_waitcnt lgkmcnt(6)
	v_mfma_f32_32x32x16_bf16 v[80:95], v[152:155], v[136:139], v[80:95]
	ds_read_b64_tr_b16 v[200:201], v177 offset:0x4600
	ds_read_b64_tr_b16 v[202:203], v177 offset:0x5600
	s_waitcnt lgkmcnt(6)
	v_mfma_f32_32x32x16_bf16 v[80:95], v[156:159], v[140:143], v[80:95]
	ds_read_b64_tr_b16 v[204:205], v177 offset:0x6600
	ds_read_b64_tr_b16 v[206:207], v177 offset:0x7600
	s_waitcnt lgkmcnt(6)
	v_mfma_f32_32x32x16_bf16 v[64:79], v[192:195], v[128:131], v[64:79]
	ds_read_b64_tr_b16 v[144:145], v177 offset:0x800
	ds_read_b64_tr_b16 v[146:147], v177 offset:0x1800
	s_waitcnt lgkmcnt(6)
	v_mfma_f32_32x32x16_bf16 v[64:79], v[196:199], v[132:135], v[64:79]
	ds_read_b64_tr_b16 v[148:149], v177 offset:0x2800
	ds_read_b64_tr_b16 v[150:151], v177 offset:0x3800
	s_waitcnt lgkmcnt(6)
	v_mfma_f32_32x32x16_bf16 v[64:79], v[200:203], v[136:139], v[64:79]
	ds_read_b64_tr_b16 v[152:153], v177 offset:0x4800
	ds_read_b64_tr_b16 v[154:155], v177 offset:0x5800
	s_waitcnt lgkmcnt(6)
	v_mfma_f32_32x32x16_bf16 v[64:79], v[204:207], v[140:143], v[64:79]
	ds_read_b64_tr_b16 v[156:157], v177 offset:0x6800
	ds_read_b64_tr_b16 v[158:159], v177 offset:0x7800
	s_waitcnt lgkmcnt(6)
	v_mfma_f32_32x32x16_bf16 v[48:63], v[144:147], v[128:131], v[48:63]
	ds_read_b64_tr_b16 v[192:193], v177 offset:0xa00
	ds_read_b64_tr_b16 v[194:195], v177 offset:0x1a00
	s_waitcnt lgkmcnt(6)
	v_mfma_f32_32x32x16_bf16 v[48:63], v[148:151], v[132:135], v[48:63]
	ds_read_b64_tr_b16 v[196:197], v177 offset:0x2a00
	ds_read_b64_tr_b16 v[198:199], v177 offset:0x3a00
	s_waitcnt lgkmcnt(6)
	v_mfma_f32_32x32x16_bf16 v[48:63], v[152:155], v[136:139], v[48:63]
	ds_read_b64_tr_b16 v[200:201], v177 offset:0x4a00
	ds_read_b64_tr_b16 v[202:203], v177 offset:0x5a00
	s_waitcnt lgkmcnt(6)
	v_mfma_f32_32x32x16_bf16 v[48:63], v[156:159], v[140:143], v[48:63]
	ds_read_b64_tr_b16 v[204:205], v177 offset:0x6a00
	ds_read_b64_tr_b16 v[206:207], v177 offset:0x7a00
	s_waitcnt lgkmcnt(6)
	v_mfma_f32_32x32x16_bf16 v[32:47], v[192:195], v[128:131], v[32:47]
	ds_read_b64_tr_b16 v[144:145], v177 offset:0xc00
	ds_read_b64_tr_b16 v[146:147], v177 offset:0x1c00
	s_waitcnt lgkmcnt(6)
	v_mfma_f32_32x32x16_bf16 v[32:47], v[196:199], v[132:135], v[32:47]
	ds_read_b64_tr_b16 v[148:149], v177 offset:0x2c00
	ds_read_b64_tr_b16 v[150:151], v177 offset:0x3c00
	s_waitcnt lgkmcnt(6)
	v_mfma_f32_32x32x16_bf16 v[32:47], v[200:203], v[136:139], v[32:47]
	ds_read_b64_tr_b16 v[152:153], v177 offset:0x4c00
	ds_read_b64_tr_b16 v[154:155], v177 offset:0x5c00
	s_waitcnt lgkmcnt(6)
	v_mfma_f32_32x32x16_bf16 v[32:47], v[204:207], v[140:143], v[32:47]
	ds_read_b64_tr_b16 v[156:157], v177 offset:0x6c00
	ds_read_b64_tr_b16 v[158:159], v177 offset:0x7c00
	s_waitcnt lgkmcnt(6)
	v_mfma_f32_32x32x16_bf16 v[16:31], v[144:147], v[128:131], v[16:31]
	ds_read_b64_tr_b16 v[192:193], v177 offset:0xe00
	ds_read_b64_tr_b16 v[194:195], v177 offset:0x1e00
	s_waitcnt lgkmcnt(6)
	v_mfma_f32_32x32x16_bf16 v[16:31], v[148:151], v[132:135], v[16:31]
	ds_read_b64_tr_b16 v[196:197], v177 offset:0x2e00
	ds_read_b64_tr_b16 v[198:199], v177 offset:0x3e00
	s_waitcnt lgkmcnt(6)
	v_mfma_f32_32x32x16_bf16 v[16:31], v[152:155], v[136:139], v[16:31]
	ds_read_b64_tr_b16 v[200:201], v177 offset:0x4e00
	ds_read_b64_tr_b16 v[202:203], v177 offset:0x5e00
	s_waitcnt lgkmcnt(6)
	v_mfma_f32_32x32x16_bf16 v[16:31], v[156:159], v[140:143], v[16:31]
	ds_read_b64_tr_b16 v[204:205], v177 offset:0x6e00
	ds_read_b64_tr_b16 v[206:207], v177 offset:0x7e00
	s_waitcnt lgkmcnt(6)
	v_mfma_f32_32x32x16_bf16 v[0:15], v[192:195], v[128:131], v[0:15]
	s_waitcnt lgkmcnt(4)
	v_mfma_f32_32x32x16_bf16 v[0:15], v[196:199], v[132:135], v[0:15]
	s_waitcnt lgkmcnt(2)
	v_mfma_f32_32x32x16_bf16 v[0:15], v[200:203], v[136:139], v[0:15]
	s_waitcnt lgkmcnt(0)
	v_mfma_f32_32x32x16_bf16 v[0:15], v[204:207], v[140:143], v[0:15]
	ds_read_b128 v[128:131], v188 offset:0
	ds_read_b128 v[132:135], v188 offset:0x2000
	ds_read_b128 v[192:195], v187 offset:0
	ds_read_b128 v[196:199], v187 offset:0x2000
	s_waitcnt lgkmcnt(2)
	s_nop 0
	v_mfma_f32_32x32x16_bf16 v[144:159], v[128:131], v[218:221], 0
	v_mfma_f32_32x32x16_bf16 v[128:143], v[132:135], v[218:221], 0
	ds_read_b128 v[204:207], v186 offset:0
	ds_read_b128 v[208:211], v186 offset:0x2000
	s_waitcnt lgkmcnt(2)
	v_mfma_f32_32x32x16_bf16 v[144:159], v[192:195], v[222:225], v[144:159]
	v_mfma_f32_32x32x16_bf16 v[128:143], v[196:199], v[222:225], v[128:143]
	ds_read_b128 v[192:195], v185 offset:0
	ds_read_b128 v[196:199], v185 offset:0x2000
	s_waitcnt lgkmcnt(2)
	v_mfma_f32_32x32x16_bf16 v[144:159], v[204:207], v[230:233], v[144:159]
	v_mfma_f32_32x32x16_bf16 v[128:143], v[208:211], v[230:233], v[128:143]
	ds_read_b128 v[204:207], v188 offset:0x80
	ds_read_b128 v[208:211], v188 offset:0x2080
	s_waitcnt lgkmcnt(2)
	v_mfma_f32_32x32x16_bf16 v[144:159], v[192:195], v[234:237], v[144:159]
	v_mfma_f32_32x32x16_bf16 v[128:143], v[196:199], v[234:237], v[128:143]
	ds_read_b128 v[192:195], v187 offset:0x80
	ds_read_b128 v[196:199], v187 offset:0x2080
	s_waitcnt lgkmcnt(2)
	v_mfma_f32_32x32x16_bf16 v[144:159], v[204:207], v[238:241], v[144:159]
	v_mfma_f32_32x32x16_bf16 v[128:143], v[208:211], v[238:241], v[128:143]
	ds_read_b128 v[204:207], v186 offset:0x80
	ds_read_b128 v[208:211], v186 offset:0x2080
	s_waitcnt lgkmcnt(2)
	v_mfma_f32_32x32x16_bf16 v[144:159], v[192:195], v[242:245], v[144:159]
	v_mfma_f32_32x32x16_bf16 v[128:143], v[196:199], v[242:245], v[128:143]
	ds_read_b128 v[192:195], v185 offset:0x80
	ds_read_b128 v[196:199], v185 offset:0x2080
	s_waitcnt lgkmcnt(2)
	v_mfma_f32_32x32x16_bf16 v[144:159], v[204:207], v[246:249], v[144:159]
	v_mfma_f32_32x32x16_bf16 v[128:143], v[208:211], v[246:249], v[128:143]
	s_waitcnt lgkmcnt(0)
	v_mfma_f32_32x32x16_bf16 v[144:159], v[192:195], v[166:169], v[144:159]
	v_mfma_f32_32x32x16_bf16 v[128:143], v[196:199], v[166:169], v[128:143]
	s_bitcmp0_b32 s100, 8
	s_cbranch_scc1 .Lstg_a18
	s_waitcnt vmcnt(0)
	s_waitcnt lgkmcnt(0)
	s_barrier
	s_sleep 5

.LBB0_597:
	ds_read_b64_tr_b16 v[144:145], v177 offset:0x8000
	ds_read_b64_tr_b16 v[146:147], v177 offset:0x9000
	ds_read_b64_tr_b16 v[148:149], v177 offset:0xa000
	ds_read_b64_tr_b16 v[150:151], v177 offset:0xb000
	ds_read_b64_tr_b16 v[152:153], v177 offset:0xc000
	ds_read_b64_tr_b16 v[154:155], v177 offset:0xd000
	ds_read_b64_tr_b16 v[156:157], v177 offset:0xe000
	ds_read_b64_tr_b16 v[158:159], v177 offset:0xf000
	s_waitcnt lgkmcnt(6)
	s_nop 0
	v_mfma_f32_32x32x16_bf16 v[112:127], v[144:147], v[128:131], v[112:127]
	ds_read_b64_tr_b16 v[194:195], v177 offset:0x8200
	ds_read_b64_tr_b16 v[196:197], v177 offset:0x9200
	s_waitcnt lgkmcnt(6)
	v_mfma_f32_32x32x16_bf16 v[112:127], v[148:151], v[132:135], v[112:127]
	ds_read_b64_tr_b16 v[198:199], v177 offset:0xa200
	ds_read_b64_tr_b16 v[200:201], v177 offset:0xb200
	s_waitcnt lgkmcnt(6)
	v_mfma_f32_32x32x16_bf16 v[112:127], v[152:155], v[136:139], v[112:127]
	ds_read_b64_tr_b16 v[202:203], v177 offset:0xc200
	ds_read_b64_tr_b16 v[204:205], v177 offset:0xd200
	s_waitcnt lgkmcnt(6)
	v_mfma_f32_32x32x16_bf16 v[112:127], v[156:159], v[140:143], v[112:127]
	ds_read_b64_tr_b16 v[206:207], v177 offset:0xe200
	ds_read_b64_tr_b16 v[208:209], v177 offset:0xf200
	s_waitcnt lgkmcnt(6)
	v_mfma_f32_32x32x16_bf16 v[96:111], v[194:197], v[128:131], v[96:111]
	ds_read_b64_tr_b16 v[144:145], v177 offset:0x8400
	ds_read_b64_tr_b16 v[146:147], v177 offset:0x9400
	s_waitcnt lgkmcnt(6)
	v_mfma_f32_32x32x16_bf16 v[96:111], v[198:201], v[132:135], v[96:111]
	ds_read_b64_tr_b16 v[148:149], v177 offset:0xa400
	ds_read_b64_tr_b16 v[150:151], v177 offset:0xb400
	s_waitcnt lgkmcnt(6)
	v_mfma_f32_32x32x16_bf16 v[96:111], v[202:205], v[136:139], v[96:111]
	ds_read_b64_tr_b16 v[152:153], v177 offset:0xc400
	ds_read_b64_tr_b16 v[154:155], v177 offset:0xd400
	s_waitcnt lgkmcnt(6)
	v_mfma_f32_32x32x16_bf16 v[96:111], v[206:209], v[140:143], v[96:111]
	ds_read_b64_tr_b16 v[156:157], v177 offset:0xe400
	ds_read_b64_tr_b16 v[158:159], v177 offset:0xf400
	s_waitcnt lgkmcnt(6)
	v_mfma_f32_32x32x16_bf16 v[80:95], v[144:147], v[128:131], v[80:95]
	ds_read_b64_tr_b16 v[194:195], v177 offset:0x8600
	ds_read_b64_tr_b16 v[196:197], v177 offset:0x9600
	s_waitcnt lgkmcnt(6)
	v_mfma_f32_32x32x16_bf16 v[80:95], v[148:151], v[132:135], v[80:95]
	ds_read_b64_tr_b16 v[198:199], v177 offset:0xa600
	ds_read_b64_tr_b16 v[200:201], v177 offset:0xb600
	s_waitcnt lgkmcnt(6)
	v_mfma_f32_32x32x16_bf16 v[80:95], v[152:155], v[136:139], v[80:95]
	ds_read_b64_tr_b16 v[202:203], v177 offset:0xc600
	ds_read_b64_tr_b16 v[204:205], v177 offset:0xd600
	s_waitcnt lgkmcnt(6)
	v_mfma_f32_32x32x16_bf16 v[80:95], v[156:159], v[140:143], v[80:95]
	ds_read_b64_tr_b16 v[206:207], v177 offset:0xe600
	ds_read_b64_tr_b16 v[208:209], v177 offset:0xf600
	s_waitcnt lgkmcnt(6)
	v_mfma_f32_32x32x16_bf16 v[64:79], v[194:197], v[128:131], v[64:79]
	ds_read_b64_tr_b16 v[144:145], v177 offset:0x8800
	ds_read_b64_tr_b16 v[146:147], v177 offset:0x9800
	s_waitcnt lgkmcnt(6)
	v_mfma_f32_32x32x16_bf16 v[64:79], v[198:201], v[132:135], v[64:79]
	ds_read_b64_tr_b16 v[148:149], v177 offset:0xa800
	ds_read_b64_tr_b16 v[150:151], v177 offset:0xb800
	s_waitcnt lgkmcnt(6)
	v_mfma_f32_32x32x16_bf16 v[64:79], v[202:205], v[136:139], v[64:79]
	ds_read_b64_tr_b16 v[152:153], v177 offset:0xc800
	ds_read_b64_tr_b16 v[154:155], v177 offset:0xd800
	s_waitcnt lgkmcnt(6)
	v_mfma_f32_32x32x16_bf16 v[64:79], v[206:209], v[140:143], v[64:79]
	ds_read_b64_tr_b16 v[156:157], v177 offset:0xe800
	ds_read_b64_tr_b16 v[158:159], v177 offset:0xf800
	s_waitcnt lgkmcnt(6)
	v_mfma_f32_32x32x16_bf16 v[48:63], v[144:147], v[128:131], v[48:63]
	ds_read_b64_tr_b16 v[194:195], v177 offset:0x8a00
	ds_read_b64_tr_b16 v[196:197], v177 offset:0x9a00
	s_waitcnt lgkmcnt(6)
	v_mfma_f32_32x32x16_bf16 v[48:63], v[148:151], v[132:135], v[48:63]
	ds_read_b64_tr_b16 v[198:199], v177 offset:0xaa00
	ds_read_b64_tr_b16 v[200:201], v177 offset:0xba00
	s_waitcnt lgkmcnt(6)
	v_mfma_f32_32x32x16_bf16 v[48:63], v[152:155], v[136:139], v[48:63]
	ds_read_b64_tr_b16 v[202:203], v177 offset:0xca00
	ds_read_b64_tr_b16 v[204:205], v177 offset:0xda00
	s_waitcnt lgkmcnt(6)
	v_mfma_f32_32x32x16_bf16 v[48:63], v[156:159], v[140:143], v[48:63]
	ds_read_b64_tr_b16 v[206:207], v177 offset:0xea00
	ds_read_b64_tr_b16 v[208:209], v177 offset:0xfa00
	s_waitcnt lgkmcnt(6)
	v_mfma_f32_32x32x16_bf16 v[32:47], v[194:197], v[128:131], v[32:47]
	ds_read_b64_tr_b16 v[144:145], v177 offset:0x8c00
	ds_read_b64_tr_b16 v[146:147], v177 offset:0x9c00
	s_waitcnt lgkmcnt(6)
	v_mfma_f32_32x32x16_bf16 v[32:47], v[198:201], v[132:135], v[32:47]
	ds_read_b64_tr_b16 v[148:149], v177 offset:0xac00
	ds_read_b64_tr_b16 v[150:151], v177 offset:0xbc00
	s_waitcnt lgkmcnt(6)
	v_mfma_f32_32x32x16_bf16 v[32:47], v[202:205], v[136:139], v[32:47]
	ds_read_b64_tr_b16 v[152:153], v177 offset:0xcc00
	ds_read_b64_tr_b16 v[154:155], v177 offset:0xdc00
	s_waitcnt lgkmcnt(6)
	v_mfma_f32_32x32x16_bf16 v[32:47], v[206:209], v[140:143], v[32:47]
	ds_read_b64_tr_b16 v[156:157], v177 offset:0xec00
	ds_read_b64_tr_b16 v[158:159], v177 offset:0xfc00
	s_waitcnt lgkmcnt(6)
	v_mfma_f32_32x32x16_bf16 v[16:31], v[144:147], v[128:131], v[16:31]
	ds_read_b64_tr_b16 v[194:195], v177 offset:0x8e00
	ds_read_b64_tr_b16 v[196:197], v177 offset:0x9e00
	s_waitcnt lgkmcnt(6)
	v_mfma_f32_32x32x16_bf16 v[16:31], v[148:151], v[132:135], v[16:31]
	ds_read_b64_tr_b16 v[198:199], v177 offset:0xae00
	ds_read_b64_tr_b16 v[200:201], v177 offset:0xbe00
	s_waitcnt lgkmcnt(6)
	v_mfma_f32_32x32x16_bf16 v[16:31], v[152:155], v[136:139], v[16:31]
	ds_read_b64_tr_b16 v[202:203], v177 offset:0xce00
	ds_read_b64_tr_b16 v[204:205], v177 offset:0xde00
	s_waitcnt lgkmcnt(6)
	v_mfma_f32_32x32x16_bf16 v[16:31], v[156:159], v[140:143], v[16:31]
	ds_read_b64_tr_b16 v[206:207], v177 offset:0xee00
	ds_read_b64_tr_b16 v[208:209], v177 offset:0xfe00
	s_waitcnt lgkmcnt(6)
	v_mfma_f32_32x32x16_bf16 v[0:15], v[194:197], v[128:131], v[0:15]
	s_waitcnt lgkmcnt(4)
	v_mfma_f32_32x32x16_bf16 v[0:15], v[198:201], v[132:135], v[0:15]
	s_waitcnt lgkmcnt(2)
	v_mfma_f32_32x32x16_bf16 v[0:15], v[202:205], v[136:139], v[0:15]
	s_waitcnt lgkmcnt(0)
	v_mfma_f32_32x32x16_bf16 v[0:15], v[206:209], v[140:143], v[0:15]
	ds_read_b128 v[128:131], v181 offset:0
	ds_read_b128 v[132:135], v181 offset:0x2000
	ds_read_b128 v[194:197], v182 offset:0
	ds_read_b128 v[198:201], v182 offset:0x2000
	s_waitcnt lgkmcnt(2)
	s_nop 0
	v_mfma_f32_32x32x16_bf16 v[144:159], v[128:131], v[218:221], 0
	v_mfma_f32_32x32x16_bf16 v[128:143], v[132:135], v[218:221], 0
	ds_read_b128 v[206:209], v183 offset:0
	ds_read_b128 v[210:213], v183 offset:0x2000
	s_waitcnt lgkmcnt(2)
	v_mfma_f32_32x32x16_bf16 v[144:159], v[194:197], v[222:225], v[144:159]
	v_mfma_f32_32x32x16_bf16 v[128:143], v[198:201], v[222:225], v[128:143]
	ds_read_b128 v[194:197], v184 offset:0
	ds_read_b128 v[198:201], v184 offset:0x2000
	s_waitcnt lgkmcnt(2)
	v_mfma_f32_32x32x16_bf16 v[144:159], v[206:209], v[230:233], v[144:159]
	v_mfma_f32_32x32x16_bf16 v[128:143], v[210:213], v[230:233], v[128:143]
	ds_read_b128 v[206:209], v181 offset:0x80
	ds_read_b128 v[210:213], v181 offset:0x2080
	s_waitcnt lgkmcnt(2)
	v_mfma_f32_32x32x16_bf16 v[144:159], v[194:197], v[234:237], v[144:159]
	v_mfma_f32_32x32x16_bf16 v[128:143], v[198:201], v[234:237], v[128:143]
	ds_read_b128 v[194:197], v182 offset:0x80
	ds_read_b128 v[198:201], v182 offset:0x2080
	s_waitcnt lgkmcnt(2)
	v_mfma_f32_32x32x16_bf16 v[144:159], v[206:209], v[238:241], v[144:159]
	v_mfma_f32_32x32x16_bf16 v[128:143], v[210:213], v[238:241], v[128:143]
	ds_read_b128 v[206:209], v183 offset:0x80
	ds_read_b128 v[210:213], v183 offset:0x2080
	s_waitcnt lgkmcnt(2)
	v_mfma_f32_32x32x16_bf16 v[144:159], v[194:197], v[242:245], v[144:159]
	v_mfma_f32_32x32x16_bf16 v[128:143], v[198:201], v[242:245], v[128:143]
	ds_read_b128 v[194:197], v184 offset:0x80
	ds_read_b128 v[198:201], v184 offset:0x2080
	s_waitcnt lgkmcnt(2)
	v_mfma_f32_32x32x16_bf16 v[144:159], v[206:209], v[246:249], v[144:159]
	v_mfma_f32_32x32x16_bf16 v[128:143], v[210:213], v[246:249], v[128:143]
	s_waitcnt lgkmcnt(0)
	v_mfma_f32_32x32x16_bf16 v[144:159], v[194:197], v[166:169], v[144:159]
	v_mfma_f32_32x32x16_bf16 v[128:143], v[198:201], v[166:169], v[128:143]
	s_bitcmp0_b32 s100, 8
	s_cbranch_scc1 .Lstg_a19
	s_waitcnt vmcnt(0)
	s_waitcnt lgkmcnt(0)
	s_barrier
	s_sleep 5

.LBB0_612:
	ds_read_b64_tr_b16 v[144:145], v177 offset:0
	ds_read_b64_tr_b16 v[146:147], v177 offset:0x1000
	ds_read_b64_tr_b16 v[148:149], v177 offset:0x2000
	ds_read_b64_tr_b16 v[150:151], v177 offset:0x3000
	ds_read_b64_tr_b16 v[152:153], v177 offset:0x4000
	ds_read_b64_tr_b16 v[154:155], v177 offset:0x5000
	ds_read_b64_tr_b16 v[156:157], v177 offset:0x6000
	ds_read_b64_tr_b16 v[158:159], v177 offset:0x7000
	s_waitcnt lgkmcnt(6)
	s_nop 0
	v_mfma_f32_32x32x16_bf16 v[112:127], v[144:147], v[128:131], v[112:127]
	ds_read_b64_tr_b16 v[192:193], v177 offset:0x200
	ds_read_b64_tr_b16 v[194:195], v177 offset:0x1200
	s_waitcnt lgkmcnt(6)
	v_mfma_f32_32x32x16_bf16 v[112:127], v[148:151], v[132:135], v[112:127]
	ds_read_b64_tr_b16 v[196:197], v177 offset:0x2200
	ds_read_b64_tr_b16 v[198:199], v177 offset:0x3200
	s_waitcnt lgkmcnt(6)
	v_mfma_f32_32x32x16_bf16 v[112:127], v[152:155], v[136:139], v[112:127]
	ds_read_b64_tr_b16 v[200:201], v177 offset:0x4200
	ds_read_b64_tr_b16 v[202:203], v177 offset:0x5200
	s_waitcnt lgkmcnt(6)
	v_mfma_f32_32x32x16_bf16 v[112:127], v[156:159], v[140:143], v[112:127]
	ds_read_b64_tr_b16 v[204:205], v177 offset:0x6200
	ds_read_b64_tr_b16 v[206:207], v177 offset:0x7200
	s_waitcnt lgkmcnt(6)
	v_mfma_f32_32x32x16_bf16 v[96:111], v[192:195], v[128:131], v[96:111]
	ds_read_b64_tr_b16 v[144:145], v177 offset:0x400
	ds_read_b64_tr_b16 v[146:147], v177 offset:0x1400
	s_waitcnt lgkmcnt(6)
	v_mfma_f32_32x32x16_bf16 v[96:111], v[196:199], v[132:135], v[96:111]
	ds_read_b64_tr_b16 v[148:149], v177 offset:0x2400
	ds_read_b64_tr_b16 v[150:151], v177 offset:0x3400
	s_waitcnt lgkmcnt(6)
	v_mfma_f32_32x32x16_bf16 v[96:111], v[200:203], v[136:139], v[96:111]
	ds_read_b64_tr_b16 v[152:153], v177 offset:0x4400
	ds_read_b64_tr_b16 v[154:155], v177 offset:0x5400
	s_waitcnt lgkmcnt(6)
	v_mfma_f32_32x32x16_bf16 v[96:111], v[204:207], v[140:143], v[96:111]
	ds_read_b64_tr_b16 v[156:157], v177 offset:0x6400
	ds_read_b64_tr_b16 v[158:159], v177 offset:0x7400
	s_waitcnt lgkmcnt(6)
	v_mfma_f32_32x32x16_bf16 v[80:95], v[144:147], v[128:131], v[80:95]
	ds_read_b64_tr_b16 v[192:193], v177 offset:0x600
	ds_read_b64_tr_b16 v[194:195], v177 offset:0x1600
	s_waitcnt lgkmcnt(6)
	v_mfma_f32_32x32x16_bf16 v[80:95], v[148:151], v[132:135], v[80:95]
	ds_read_b64_tr_b16 v[196:197], v177 offset:0x2600
	ds_read_b64_tr_b16 v[198:199], v177 offset:0x3600
	s_waitcnt lgkmcnt(6)
	v_mfma_f32_32x32x16_bf16 v[80:95], v[152:155], v[136:139], v[80:95]
	ds_read_b64_tr_b16 v[200:201], v177 offset:0x4600
	ds_read_b64_tr_b16 v[202:203], v177 offset:0x5600
	s_waitcnt lgkmcnt(6)
	v_mfma_f32_32x32x16_bf16 v[80:95], v[156:159], v[140:143], v[80:95]
	ds_read_b64_tr_b16 v[204:205], v177 offset:0x6600
	ds_read_b64_tr_b16 v[206:207], v177 offset:0x7600
	s_waitcnt lgkmcnt(6)
	v_mfma_f32_32x32x16_bf16 v[64:79], v[192:195], v[128:131], v[64:79]
	ds_read_b64_tr_b16 v[144:145], v177 offset:0x800
	ds_read_b64_tr_b16 v[146:147], v177 offset:0x1800
	s_waitcnt lgkmcnt(6)
	v_mfma_f32_32x32x16_bf16 v[64:79], v[196:199], v[132:135], v[64:79]
	ds_read_b64_tr_b16 v[148:149], v177 offset:0x2800
	ds_read_b64_tr_b16 v[150:151], v177 offset:0x3800
	s_waitcnt lgkmcnt(6)
	v_mfma_f32_32x32x16_bf16 v[64:79], v[200:203], v[136:139], v[64:79]
	ds_read_b64_tr_b16 v[152:153], v177 offset:0x4800
	ds_read_b64_tr_b16 v[154:155], v177 offset:0x5800
	s_waitcnt lgkmcnt(6)
	v_mfma_f32_32x32x16_bf16 v[64:79], v[204:207], v[140:143], v[64:79]
	ds_read_b64_tr_b16 v[156:157], v177 offset:0x6800
	ds_read_b64_tr_b16 v[158:159], v177 offset:0x7800
	s_waitcnt lgkmcnt(6)
	v_mfma_f32_32x32x16_bf16 v[48:63], v[144:147], v[128:131], v[48:63]
	ds_read_b64_tr_b16 v[192:193], v177 offset:0xa00
	ds_read_b64_tr_b16 v[194:195], v177 offset:0x1a00
	s_waitcnt lgkmcnt(6)
	v_mfma_f32_32x32x16_bf16 v[48:63], v[148:151], v[132:135], v[48:63]
	ds_read_b64_tr_b16 v[196:197], v177 offset:0x2a00
	ds_read_b64_tr_b16 v[198:199], v177 offset:0x3a00
	s_waitcnt lgkmcnt(6)
	v_mfma_f32_32x32x16_bf16 v[48:63], v[152:155], v[136:139], v[48:63]
	ds_read_b64_tr_b16 v[200:201], v177 offset:0x4a00
	ds_read_b64_tr_b16 v[202:203], v177 offset:0x5a00
	s_waitcnt lgkmcnt(6)
	v_mfma_f32_32x32x16_bf16 v[48:63], v[156:159], v[140:143], v[48:63]
	ds_read_b64_tr_b16 v[204:205], v177 offset:0x6a00
	ds_read_b64_tr_b16 v[206:207], v177 offset:0x7a00
	s_waitcnt lgkmcnt(6)
	v_mfma_f32_32x32x16_bf16 v[32:47], v[192:195], v[128:131], v[32:47]
	ds_read_b64_tr_b16 v[144:145], v177 offset:0xc00
	ds_read_b64_tr_b16 v[146:147], v177 offset:0x1c00
	s_waitcnt lgkmcnt(6)
	v_mfma_f32_32x32x16_bf16 v[32:47], v[196:199], v[132:135], v[32:47]
	ds_read_b64_tr_b16 v[148:149], v177 offset:0x2c00
	ds_read_b64_tr_b16 v[150:151], v177 offset:0x3c00
	s_waitcnt lgkmcnt(6)
	v_mfma_f32_32x32x16_bf16 v[32:47], v[200:203], v[136:139], v[32:47]
	ds_read_b64_tr_b16 v[152:153], v177 offset:0x4c00
	ds_read_b64_tr_b16 v[154:155], v177 offset:0x5c00
	s_waitcnt lgkmcnt(6)
	v_mfma_f32_32x32x16_bf16 v[32:47], v[204:207], v[140:143], v[32:47]
	ds_read_b64_tr_b16 v[156:157], v177 offset:0x6c00
	ds_read_b64_tr_b16 v[158:159], v177 offset:0x7c00
	s_waitcnt lgkmcnt(6)
	v_mfma_f32_32x32x16_bf16 v[16:31], v[144:147], v[128:131], v[16:31]
	ds_read_b64_tr_b16 v[192:193], v177 offset:0xe00
	ds_read_b64_tr_b16 v[194:195], v177 offset:0x1e00
	s_waitcnt lgkmcnt(6)
	v_mfma_f32_32x32x16_bf16 v[16:31], v[148:151], v[132:135], v[16:31]
	ds_read_b64_tr_b16 v[196:197], v177 offset:0x2e00
	ds_read_b64_tr_b16 v[198:199], v177 offset:0x3e00
	s_waitcnt lgkmcnt(6)
	v_mfma_f32_32x32x16_bf16 v[16:31], v[152:155], v[136:139], v[16:31]
	ds_read_b64_tr_b16 v[200:201], v177 offset:0x4e00
	ds_read_b64_tr_b16 v[202:203], v177 offset:0x5e00
	s_waitcnt lgkmcnt(6)
	v_mfma_f32_32x32x16_bf16 v[16:31], v[156:159], v[140:143], v[16:31]
	ds_read_b64_tr_b16 v[204:205], v177 offset:0x6e00
	ds_read_b64_tr_b16 v[206:207], v177 offset:0x7e00
	s_waitcnt lgkmcnt(6)
	v_mfma_f32_32x32x16_bf16 v[0:15], v[192:195], v[128:131], v[0:15]
	s_waitcnt lgkmcnt(4)
	v_mfma_f32_32x32x16_bf16 v[0:15], v[196:199], v[132:135], v[0:15]
	s_waitcnt lgkmcnt(2)
	v_mfma_f32_32x32x16_bf16 v[0:15], v[200:203], v[136:139], v[0:15]
	s_waitcnt lgkmcnt(0)
	v_mfma_f32_32x32x16_bf16 v[0:15], v[204:207], v[140:143], v[0:15]
	ds_read_b128 v[128:131], v188 offset:0
	ds_read_b128 v[132:135], v188 offset:0x2000
	ds_read_b128 v[192:195], v187 offset:0
	ds_read_b128 v[196:199], v187 offset:0x2000
	s_waitcnt lgkmcnt(2)
	s_nop 0
	v_mfma_f32_32x32x16_bf16 v[144:159], v[128:131], v[218:221], 0
	v_mfma_f32_32x32x16_bf16 v[128:143], v[132:135], v[218:221], 0
	ds_read_b128 v[204:207], v186 offset:0
	ds_read_b128 v[208:211], v186 offset:0x2000
	s_waitcnt lgkmcnt(2)
	v_mfma_f32_32x32x16_bf16 v[144:159], v[192:195], v[222:225], v[144:159]
	v_mfma_f32_32x32x16_bf16 v[128:143], v[196:199], v[222:225], v[128:143]
	ds_read_b128 v[192:195], v185 offset:0
	ds_read_b128 v[196:199], v185 offset:0x2000
	s_waitcnt lgkmcnt(2)
	v_mfma_f32_32x32x16_bf16 v[144:159], v[204:207], v[230:233], v[144:159]
	v_mfma_f32_32x32x16_bf16 v[128:143], v[208:211], v[230:233], v[128:143]
	ds_read_b128 v[204:207], v188 offset:0x80
	ds_read_b128 v[208:211], v188 offset:0x2080
	s_waitcnt lgkmcnt(2)
	v_mfma_f32_32x32x16_bf16 v[144:159], v[192:195], v[234:237], v[144:159]
	v_mfma_f32_32x32x16_bf16 v[128:143], v[196:199], v[234:237], v[128:143]
	ds_read_b128 v[192:195], v187 offset:0x80
	ds_read_b128 v[196:199], v187 offset:0x2080
	s_waitcnt lgkmcnt(2)
	v_mfma_f32_32x32x16_bf16 v[144:159], v[204:207], v[238:241], v[144:159]
	v_mfma_f32_32x32x16_bf16 v[128:143], v[208:211], v[238:241], v[128:143]
	ds_read_b128 v[204:207], v186 offset:0x80
	ds_read_b128 v[208:211], v186 offset:0x2080
	s_waitcnt lgkmcnt(2)
	v_mfma_f32_32x32x16_bf16 v[144:159], v[192:195], v[242:245], v[144:159]
	v_mfma_f32_32x32x16_bf16 v[128:143], v[196:199], v[242:245], v[128:143]
	ds_read_b128 v[180:183], v185 offset:0x80
	ds_read_b128 v[192:195], v185 offset:0x2080
	s_waitcnt lgkmcnt(2)
	v_mfma_f32_32x32x16_bf16 v[144:159], v[204:207], v[246:249], v[144:159]
	v_mfma_f32_32x32x16_bf16 v[128:143], v[208:211], v[246:249], v[128:143]
	s_waitcnt lgkmcnt(0)
	v_mfma_f32_32x32x16_bf16 v[144:159], v[180:183], v[166:169], v[144:159]
	v_mfma_f32_32x32x16_bf16 v[128:143], v[192:195], v[166:169], v[128:143]
	s_bitcmp0_b32 s100, 8
	s_cbranch_scc1 .Lstg_a20
	s_waitcnt vmcnt(0)
	s_waitcnt lgkmcnt(0)
	s_barrier
	s_sleep 5
